# early-start gather: first-chunk hits loaded before full scan/sort; D=16; finalize kernargs loaded up front
# speedup vs baseline: 1.0083x; 1.0083x over previous
_Z7vq_mainPKfPKiS0_PfPhPdPi:
	s_load_dwordx4 s[4:7], s[0:1], 0x0
	s_load_dwordx2 s[22:23], s[0:1], 0x10
	s_load_dwordx2 s[20:21], s[0:1], 0x18
	s_load_dwordx4 s[12:15], s[0:1], 0x20
	s_load_dwordx2 s[10:11], s[0:1], 0x30
	s_and_b32 s3, s2, 7
	s_lshl_b32 s3, s3, 6
	s_lshr_b32 s16, s2, 3
	s_add_i32 s16, s16, s3
	s_lshr_b32 s18, s16, 5
	s_mov_b32 s19, 0
	s_and_b32 s28, s16, 31
	s_lshl_b32 s28, s28, 4
	s_add_i32 s29, s28, 1
	v_readfirstlane_b32 s17, v0
	v_and_b32_e32 v1, 63, v0
	v_lshlrev_b32_e32 v224, 4, v0
	s_lshr_b32 s17, s17, 6
	s_lshl_b32 s24, s17, 4
	s_lshl_b32 s30, s18, 15
	s_lshl_b32 s31, s18, 23
	v_add_u32_e32 v225, 0x1000, v224
	v_add_u32_e32 v226, 0x2000, v224
	v_add_u32_e32 v227, 0x3000, v224
	v_add_u32_e32 v228, 0x4000, v224
	v_add_u32_e32 v229, 0x5000, v224
	v_add_u32_e32 v230, 0x6000, v224
	v_add_u32_e32 v231, 0x7000, v224
	s_waitcnt lgkmcnt(0)
	s_add_u32 s34, s6, s30
	s_addc_u32 s35, s7, 0
	s_add_u32 s32, s4, s31
	s_addc_u32 s33, s5, 0
	v_and_b32_e32 v198, 15, v0
	v_or_b32_e32 v198, s24, v198
	v_and_b32_e32 v199, 48, v0
	v_lshl_or_b32 v198, v198, 10, v199
	global_load_dwordx4 v[62:65], v198, s[22:23] offset:0
	global_load_dwordx4 v[58:61], v198, s[22:23] offset:64
	global_load_dwordx4 v[54:57], v198, s[22:23] offset:128
	global_load_dwordx4 v[50:53], v198, s[22:23] offset:192
	global_load_dwordx4 v[46:49], v198, s[22:23] offset:256
	global_load_dwordx4 v[42:45], v198, s[22:23] offset:320
	global_load_dwordx4 v[38:41], v198, s[22:23] offset:384
	global_load_dwordx4 v[34:37], v198, s[22:23] offset:448
	global_load_dwordx4 v[30:33], v198, s[22:23] offset:512
	global_load_dwordx4 v[26:29], v198, s[22:23] offset:576
	global_load_dwordx4 v[22:25], v198, s[22:23] offset:640
	global_load_dwordx4 v[18:21], v198, s[22:23] offset:704
	global_load_dwordx4 v[14:17], v198, s[22:23] offset:768
	global_load_dwordx4 v[10:13], v198, s[22:23] offset:832
	global_load_dwordx4 v[6:9], v198, s[22:23] offset:896
	global_load_dwordx4 v[2:5], v198, s[22:23] offset:960
	global_load_dwordx4 v[130:133], v224, s[34:35]
	global_load_dwordx4 v[134:137], v225, s[34:35]
	global_load_dwordx4 v[138:141], v226, s[34:35]
	global_load_dwordx4 v[142:145], v227, s[34:35]
	global_load_dwordx4 v[146:149], v228, s[34:35]
	global_load_dwordx4 v[150:153], v229, s[34:35]
	global_load_dwordx4 v[154:157], v230, s[34:35]
	global_load_dwordx4 v[158:161], v231, s[34:35]
	v_mov_b32_e32 v194, 1
	v_mov_b32_e32 v195, 4
	v_mov_b32_e32 v196, 0x11100
	v_lshlrev_b32_e32 v197, 8, v0
	v_lshlrev_b32_e32 v222, 3, v0
	v_lshlrev_b32_e32 v218, 4, v1
	v_lshlrev_b32_e32 v219, 3, v1
	v_mov_b32_e32 v234, 0
	v_mov_b32_e32 v235, 0
	v_mov_b32_e32 v232, 0
	ds_write_b64 v222, v[234:235] offset:32768
	ds_write_b64 v222, v[234:235] offset:34832
	ds_write_b64 v222, v[234:235] offset:36896
	ds_write_b64 v222, v[234:235] offset:38960
	ds_write_b64 v222, v[234:235] offset:41024
	ds_write_b64 v222, v[234:235] offset:43088
	ds_write_b64 v222, v[234:235] offset:45152
	ds_write_b64 v222, v[234:235] offset:47216
	ds_write_b64 v222, v[234:235] offset:49280
	ds_write_b64 v222, v[234:235] offset:51344
	ds_write_b64 v222, v[234:235] offset:53408
	ds_write_b64 v222, v[234:235] offset:55472
	ds_write_b64 v222, v[234:235] offset:57536
	ds_write_b64 v222, v[234:235] offset:59600
	ds_write_b64 v222, v[234:235] offset:61664
	ds_write_b64 v222, v[234:235] offset:63728
	v_cmp_gt_u32_e32 vcc, 16, v0
	s_and_saveexec_b64 s[30:31], vcc
	v_lshl_add_u32 v228, v0, 2, v196
	ds_write_b32 v228, v234
	ds_write_b32 v228, v234 offset:1024
	s_mov_b64 exec, s[30:31]
	s_lshl_b32 s84, s17, 8
	s_mov_b32 s9, 0
	s_waitcnt lgkmcnt(0)
	s_barrier
	s_waitcnt vmcnt(0)
	v_subrev_u32_e32 v130, s29, v130
	v_subrev_u32_e32 v131, s29, v131
	v_subrev_u32_e32 v132, s29, v132
	v_subrev_u32_e32 v133, s29, v133
	v_cmp_gt_u32_e64 s[36:37], 16, v130
	v_cmp_gt_u32_e64 s[38:39], 16, v131
	v_cmp_gt_u32_e64 s[40:41], 16, v132
	v_cmp_gt_u32_e64 s[42:43], 16, v133
	s_andn2_b64 s[88:89], s[38:39], s[36:37]
	s_or_b64 s[94:95], s[36:37], s[38:39]
	s_andn2_b64 s[90:91], s[40:41], s[94:95]
	s_or_b64 s[94:95], s[94:95], s[40:41]
	s_andn2_b64 s[92:93], s[42:43], s[94:95]
	s_or_b64 s[96:97], s[94:95], s[42:43]
	s_mov_b64 s[98:99], s[96:97]
	v_add_u32_e32 v223, 48, v133
	v_add_u32_e32 v229, 32, v132
	v_cndmask_b32_e64 v223, v223, v229, s[90:91]
	v_add_u32_e32 v229, 16, v131
	v_cndmask_b32_e64 v223, v223, v229, s[88:89]
	v_cndmask_b32_e64 v223, v223, v130, s[36:37]
	s_cmp_eq_u64 s[96:97], 0
	s_cbranch_scc1 .Le_done
	s_ff1_i32_b64 s80, s[96:97]
	s_bitset0_b64 s[96:97], s80
	v_readlane_b32 s81, v223, s80
	s_and_b32 s82, s81, 15
	v_writelane_b32 v232, s82, 0
	s_lshr_b32 s81, s81, 4
	s_lshl_b32 s83, s80, 2
	s_add_u32 s81, s81, s83
	s_add_u32 s81, s81, s84
	s_lshl_b32 s81, s81, 10
	s_add_u32 s86, s32, s81
	s_addc_u32 s87, s33, 0
	global_load_dwordx4 v[66:69], v218, s[86:87] nt
	s_mov_b32 s9, 1
	s_cmp_eq_u64 s[96:97], 0
	s_cbranch_scc1 .Le_done
	s_ff1_i32_b64 s80, s[96:97]
	s_bitset0_b64 s[96:97], s80
	v_readlane_b32 s81, v223, s80
	s_and_b32 s82, s81, 15
	v_writelane_b32 v232, s82, 1
	s_lshr_b32 s81, s81, 4
	s_lshl_b32 s83, s80, 2
	s_add_u32 s81, s81, s83
	s_add_u32 s81, s81, s84
	s_lshl_b32 s81, s81, 10
	s_add_u32 s86, s32, s81
	s_addc_u32 s87, s33, 0
	global_load_dwordx4 v[70:73], v218, s[86:87] nt
	s_mov_b32 s9, 2
	s_cmp_eq_u64 s[96:97], 0
	s_cbranch_scc1 .Le_done
	s_ff1_i32_b64 s80, s[96:97]
	s_bitset0_b64 s[96:97], s80
	v_readlane_b32 s81, v223, s80
	s_and_b32 s82, s81, 15
	v_writelane_b32 v232, s82, 2
	s_lshr_b32 s81, s81, 4
	s_lshl_b32 s83, s80, 2
	s_add_u32 s81, s81, s83
	s_add_u32 s81, s81, s84
	s_lshl_b32 s81, s81, 10
	s_add_u32 s86, s32, s81
	s_addc_u32 s87, s33, 0
	global_load_dwordx4 v[74:77], v218, s[86:87] nt
	s_mov_b32 s9, 3
	s_cmp_eq_u64 s[96:97], 0
	s_cbranch_scc1 .Le_done
	s_ff1_i32_b64 s80, s[96:97]
	s_bitset0_b64 s[96:97], s80
	v_readlane_b32 s81, v223, s80
	s_and_b32 s82, s81, 15
	v_writelane_b32 v232, s82, 3
	s_lshr_b32 s81, s81, 4
	s_lshl_b32 s83, s80, 2
	s_add_u32 s81, s81, s83
	s_add_u32 s81, s81, s84
	s_lshl_b32 s81, s81, 10
	s_add_u32 s86, s32, s81
	s_addc_u32 s87, s33, 0
	global_load_dwordx4 v[78:81], v218, s[86:87] nt
	s_mov_b32 s9, 4
	s_cmp_eq_u64 s[96:97], 0
	s_cbranch_scc1 .Le_done
	s_ff1_i32_b64 s80, s[96:97]
	s_bitset0_b64 s[96:97], s80
	v_readlane_b32 s81, v223, s80
	s_and_b32 s82, s81, 15
	v_writelane_b32 v232, s82, 4
	s_lshr_b32 s81, s81, 4
	s_lshl_b32 s83, s80, 2
	s_add_u32 s81, s81, s83
	s_add_u32 s81, s81, s84
	s_lshl_b32 s81, s81, 10
	s_add_u32 s86, s32, s81
	s_addc_u32 s87, s33, 0
	global_load_dwordx4 v[82:85], v218, s[86:87] nt
	s_mov_b32 s9, 5
	s_cmp_eq_u64 s[96:97], 0
	s_cbranch_scc1 .Le_done
	s_ff1_i32_b64 s80, s[96:97]
	s_bitset0_b64 s[96:97], s80
	v_readlane_b32 s81, v223, s80
	s_and_b32 s82, s81, 15
	v_writelane_b32 v232, s82, 5
	s_lshr_b32 s81, s81, 4
	s_lshl_b32 s83, s80, 2
	s_add_u32 s81, s81, s83
	s_add_u32 s81, s81, s84
	s_lshl_b32 s81, s81, 10
	s_add_u32 s86, s32, s81
	s_addc_u32 s87, s33, 0
	global_load_dwordx4 v[86:89], v218, s[86:87] nt
	s_mov_b32 s9, 6
	s_cmp_eq_u64 s[96:97], 0
	s_cbranch_scc1 .Le_done
	s_ff1_i32_b64 s80, s[96:97]
	s_bitset0_b64 s[96:97], s80
	v_readlane_b32 s81, v223, s80
	s_and_b32 s82, s81, 15
	v_writelane_b32 v232, s82, 6
	s_lshr_b32 s81, s81, 4
	s_lshl_b32 s83, s80, 2
	s_add_u32 s81, s81, s83
	s_add_u32 s81, s81, s84
	s_lshl_b32 s81, s81, 10
	s_add_u32 s86, s32, s81
	s_addc_u32 s87, s33, 0
	global_load_dwordx4 v[90:93], v218, s[86:87] nt
	s_mov_b32 s9, 7
	s_cmp_eq_u64 s[96:97], 0
	s_cbranch_scc1 .Le_done
	s_ff1_i32_b64 s80, s[96:97]
	s_bitset0_b64 s[96:97], s80
	v_readlane_b32 s81, v223, s80
	s_and_b32 s82, s81, 15
	v_writelane_b32 v232, s82, 7
	s_lshr_b32 s81, s81, 4
	s_lshl_b32 s83, s80, 2
	s_add_u32 s81, s81, s83
	s_add_u32 s81, s81, s84
	s_lshl_b32 s81, s81, 10
	s_add_u32 s86, s32, s81
	s_addc_u32 s87, s33, 0
	global_load_dwordx4 v[94:97], v218, s[86:87] nt
	s_mov_b32 s9, 8
	s_cmp_eq_u64 s[96:97], 0
	s_cbranch_scc1 .Le_done
	s_ff1_i32_b64 s80, s[96:97]
	s_bitset0_b64 s[96:97], s80
	v_readlane_b32 s81, v223, s80
	s_and_b32 s82, s81, 15
	v_writelane_b32 v232, s82, 8
	s_lshr_b32 s81, s81, 4
	s_lshl_b32 s83, s80, 2
	s_add_u32 s81, s81, s83
	s_add_u32 s81, s81, s84
	s_lshl_b32 s81, s81, 10
	s_add_u32 s86, s32, s81
	s_addc_u32 s87, s33, 0
	global_load_dwordx4 v[98:101], v218, s[86:87] nt
	s_mov_b32 s9, 9
	s_cmp_eq_u64 s[96:97], 0
	s_cbranch_scc1 .Le_done
	s_ff1_i32_b64 s80, s[96:97]
	s_bitset0_b64 s[96:97], s80
	v_readlane_b32 s81, v223, s80
	s_and_b32 s82, s81, 15
	v_writelane_b32 v232, s82, 9
	s_lshr_b32 s81, s81, 4
	s_lshl_b32 s83, s80, 2
	s_add_u32 s81, s81, s83
	s_add_u32 s81, s81, s84
	s_lshl_b32 s81, s81, 10
	s_add_u32 s86, s32, s81
	s_addc_u32 s87, s33, 0
	global_load_dwordx4 v[102:105], v218, s[86:87] nt
	s_mov_b32 s9, 10
	s_cmp_eq_u64 s[96:97], 0
	s_cbranch_scc1 .Le_done
	s_ff1_i32_b64 s80, s[96:97]
	s_bitset0_b64 s[96:97], s80
	v_readlane_b32 s81, v223, s80
	s_and_b32 s82, s81, 15
	v_writelane_b32 v232, s82, 10
	s_lshr_b32 s81, s81, 4
	s_lshl_b32 s83, s80, 2
	s_add_u32 s81, s81, s83
	s_add_u32 s81, s81, s84
	s_lshl_b32 s81, s81, 10
	s_add_u32 s86, s32, s81
	s_addc_u32 s87, s33, 0
	global_load_dwordx4 v[106:109], v218, s[86:87] nt
	s_mov_b32 s9, 11
	s_cmp_eq_u64 s[96:97], 0
	s_cbranch_scc1 .Le_done
	s_ff1_i32_b64 s80, s[96:97]
	s_bitset0_b64 s[96:97], s80
	v_readlane_b32 s81, v223, s80
	s_and_b32 s82, s81, 15
	v_writelane_b32 v232, s82, 11
	s_lshr_b32 s81, s81, 4
	s_lshl_b32 s83, s80, 2
	s_add_u32 s81, s81, s83
	s_add_u32 s81, s81, s84
	s_lshl_b32 s81, s81, 10
	s_add_u32 s86, s32, s81
	s_addc_u32 s87, s33, 0
	global_load_dwordx4 v[110:113], v218, s[86:87] nt
	s_mov_b32 s9, 12
	s_cmp_eq_u64 s[96:97], 0
	s_cbranch_scc1 .Le_done
	s_ff1_i32_b64 s80, s[96:97]
	s_bitset0_b64 s[96:97], s80
	v_readlane_b32 s81, v223, s80
	s_and_b32 s82, s81, 15
	v_writelane_b32 v232, s82, 12
	s_lshr_b32 s81, s81, 4
	s_lshl_b32 s83, s80, 2
	s_add_u32 s81, s81, s83
	s_add_u32 s81, s81, s84
	s_lshl_b32 s81, s81, 10
	s_add_u32 s86, s32, s81
	s_addc_u32 s87, s33, 0
	global_load_dwordx4 v[114:117], v218, s[86:87] nt
	s_mov_b32 s9, 13
	s_cmp_eq_u64 s[96:97], 0
	s_cbranch_scc1 .Le_done
	s_ff1_i32_b64 s80, s[96:97]
	s_bitset0_b64 s[96:97], s80
	v_readlane_b32 s81, v223, s80
	s_and_b32 s82, s81, 15
	v_writelane_b32 v232, s82, 13
	s_lshr_b32 s81, s81, 4
	s_lshl_b32 s83, s80, 2
	s_add_u32 s81, s81, s83
	s_add_u32 s81, s81, s84
	s_lshl_b32 s81, s81, 10
	s_add_u32 s86, s32, s81
	s_addc_u32 s87, s33, 0
	global_load_dwordx4 v[118:121], v218, s[86:87] nt
	s_mov_b32 s9, 14
	s_cmp_eq_u64 s[96:97], 0
	s_cbranch_scc1 .Le_done
	s_ff1_i32_b64 s80, s[96:97]
	s_bitset0_b64 s[96:97], s80
	v_readlane_b32 s81, v223, s80
	s_and_b32 s82, s81, 15
	v_writelane_b32 v232, s82, 14
	s_lshr_b32 s81, s81, 4
	s_lshl_b32 s83, s80, 2
	s_add_u32 s81, s81, s83
	s_add_u32 s81, s81, s84
	s_lshl_b32 s81, s81, 10
	s_add_u32 s86, s32, s81
	s_addc_u32 s87, s33, 0
	global_load_dwordx4 v[122:125], v218, s[86:87] nt
	s_mov_b32 s9, 15
	s_cmp_eq_u64 s[96:97], 0
	s_cbranch_scc1 .Le_done
	s_ff1_i32_b64 s80, s[96:97]
	s_bitset0_b64 s[96:97], s80
	v_readlane_b32 s81, v223, s80
	s_and_b32 s82, s81, 15
	v_writelane_b32 v232, s82, 15
	s_lshr_b32 s81, s81, 4
	s_lshl_b32 s83, s80, 2
	s_add_u32 s81, s81, s83
	s_add_u32 s81, s81, s84
	s_lshl_b32 s81, s81, 10
	s_add_u32 s86, s32, s81
	s_addc_u32 s87, s33, 0
	global_load_dwordx4 v[126:129], v218, s[86:87] nt
	s_mov_b32 s9, 16
.Le_done:
	s_andn2_b64 s[98:99], s[98:99], s[96:97]
	s_and_b64 s[94:95], s[36:37], s[98:99]
	s_andn2_b64 s[36:37], s[36:37], s[94:95]
	s_and_b64 s[94:95], s[88:89], s[98:99]
	s_andn2_b64 s[38:39], s[38:39], s[94:95]
	s_and_b64 s[94:95], s[90:91], s[98:99]
	s_andn2_b64 s[40:41], s[40:41], s[94:95]
	s_and_b64 s[94:95], s[92:93], s[98:99]
	s_andn2_b64 s[42:43], s[42:43], s[94:95]
	s_mov_b64 exec, s[98:99]
	v_and_b32_e32 v229, 15, v223
	v_lshl_add_u32 v229, v229, 2, v196
	ds_add_u32 v229, v194 offset:1024
	s_mov_b64 exec, -1
	v_subrev_u32_e32 v134, s29, v134
	v_subrev_u32_e32 v135, s29, v135
	v_subrev_u32_e32 v136, s29, v136
	v_subrev_u32_e32 v137, s29, v137
	v_subrev_u32_e32 v138, s29, v138
	v_subrev_u32_e32 v139, s29, v139
	v_subrev_u32_e32 v140, s29, v140
	v_subrev_u32_e32 v141, s29, v141
	v_subrev_u32_e32 v142, s29, v142
	v_subrev_u32_e32 v143, s29, v143
	v_subrev_u32_e32 v144, s29, v144
	v_subrev_u32_e32 v145, s29, v145
	v_subrev_u32_e32 v146, s29, v146
	v_subrev_u32_e32 v147, s29, v147
	v_subrev_u32_e32 v148, s29, v148
	v_subrev_u32_e32 v149, s29, v149
	v_subrev_u32_e32 v150, s29, v150
	v_subrev_u32_e32 v151, s29, v151
	v_subrev_u32_e32 v152, s29, v152
	v_subrev_u32_e32 v153, s29, v153
	v_subrev_u32_e32 v154, s29, v154
	v_subrev_u32_e32 v155, s29, v155
	v_subrev_u32_e32 v156, s29, v156
	v_subrev_u32_e32 v157, s29, v157
	v_subrev_u32_e32 v158, s29, v158
	v_subrev_u32_e32 v159, s29, v159
	v_subrev_u32_e32 v160, s29, v160
	v_subrev_u32_e32 v161, s29, v161
	v_cmp_gt_u32_e64 s[44:45], 16, v134
	v_cmp_gt_u32_e64 s[46:47], 16, v135
	v_cmp_gt_u32_e64 s[48:49], 16, v136
	v_cmp_gt_u32_e64 s[50:51], 16, v137
	v_cmp_gt_u32_e64 s[52:53], 16, v138
	v_cmp_gt_u32_e64 s[54:55], 16, v139
	v_cmp_gt_u32_e64 s[56:57], 16, v140
	v_cmp_gt_u32_e64 s[58:59], 16, v141
	v_cmp_gt_u32_e64 s[60:61], 16, v142
	v_cmp_gt_u32_e64 s[62:63], 16, v143
	v_cmp_gt_u32_e64 s[64:65], 16, v144
	v_cmp_gt_u32_e64 s[66:67], 16, v145
	v_cmp_gt_u32_e64 s[68:69], 16, v146
	v_cmp_gt_u32_e64 s[70:71], 16, v147
	v_cmp_gt_u32_e64 s[72:73], 16, v148
	v_cmp_gt_u32_e64 s[74:75], 16, v149
	v_cmp_gt_u32_e64 s[76:77], 16, v150
	v_cmp_gt_u32_e64 s[78:79], 16, v151
	v_cmp_gt_u32_e64 s[80:81], 16, v152
	v_cmp_gt_u32_e64 s[82:83], 16, v153
	v_cmp_gt_u32_e64 s[84:85], 16, v154
	v_cmp_gt_u32_e64 s[86:87], 16, v155
	v_cmp_gt_u32_e64 s[88:89], 16, v156
	v_cmp_gt_u32_e64 s[90:91], 16, v157
	v_cmp_gt_u32_e64 s[92:93], 16, v158
	v_cmp_gt_u32_e64 s[94:95], 16, v159
	v_cmp_gt_u32_e64 s[96:97], 16, v160
	v_cmp_gt_u32_e64 s[98:99], 16, v161
	s_mov_b64 exec, s[36:37]
	v_lshl_add_u32 v130, v130, 2, v196
	ds_add_u32 v130, v194
	s_mov_b64 exec, s[38:39]
	v_lshl_add_u32 v131, v131, 2, v196
	ds_add_u32 v131, v194
	s_mov_b64 exec, s[40:41]
	v_lshl_add_u32 v132, v132, 2, v196
	ds_add_u32 v132, v194
	s_mov_b64 exec, s[42:43]
	v_lshl_add_u32 v133, v133, 2, v196
	ds_add_u32 v133, v194
	s_mov_b64 exec, s[44:45]
	v_lshl_add_u32 v134, v134, 2, v196
	ds_add_u32 v134, v194
	s_mov_b64 exec, s[46:47]
	v_lshl_add_u32 v135, v135, 2, v196
	ds_add_u32 v135, v194
	s_mov_b64 exec, s[48:49]
	v_lshl_add_u32 v136, v136, 2, v196
	ds_add_u32 v136, v194
	s_mov_b64 exec, s[50:51]
	v_lshl_add_u32 v137, v137, 2, v196
	ds_add_u32 v137, v194
	s_mov_b64 exec, s[52:53]
	v_lshl_add_u32 v138, v138, 2, v196
	ds_add_u32 v138, v194
	s_mov_b64 exec, s[54:55]
	v_lshl_add_u32 v139, v139, 2, v196
	ds_add_u32 v139, v194
	s_mov_b64 exec, s[56:57]
	v_lshl_add_u32 v140, v140, 2, v196
	ds_add_u32 v140, v194
	s_mov_b64 exec, s[58:59]
	v_lshl_add_u32 v141, v141, 2, v196
	ds_add_u32 v141, v194
	s_mov_b64 exec, s[60:61]
	v_lshl_add_u32 v142, v142, 2, v196
	ds_add_u32 v142, v194
	s_mov_b64 exec, s[62:63]
	v_lshl_add_u32 v143, v143, 2, v196
	ds_add_u32 v143, v194
	s_mov_b64 exec, s[64:65]
	v_lshl_add_u32 v144, v144, 2, v196
	ds_add_u32 v144, v194
	s_mov_b64 exec, s[66:67]
	v_lshl_add_u32 v145, v145, 2, v196
	ds_add_u32 v145, v194
	s_mov_b64 exec, s[68:69]
	v_lshl_add_u32 v146, v146, 2, v196
	ds_add_u32 v146, v194
	s_mov_b64 exec, s[70:71]
	v_lshl_add_u32 v147, v147, 2, v196
	ds_add_u32 v147, v194
	s_mov_b64 exec, s[72:73]
	v_lshl_add_u32 v148, v148, 2, v196
	ds_add_u32 v148, v194
	s_mov_b64 exec, s[74:75]
	v_lshl_add_u32 v149, v149, 2, v196
	ds_add_u32 v149, v194
	s_mov_b64 exec, s[76:77]
	v_lshl_add_u32 v150, v150, 2, v196
	ds_add_u32 v150, v194
	s_mov_b64 exec, s[78:79]
	v_lshl_add_u32 v151, v151, 2, v196
	ds_add_u32 v151, v194
	s_mov_b64 exec, s[80:81]
	v_lshl_add_u32 v152, v152, 2, v196
	ds_add_u32 v152, v194
	s_mov_b64 exec, s[82:83]
	v_lshl_add_u32 v153, v153, 2, v196
	ds_add_u32 v153, v194
	s_mov_b64 exec, s[84:85]
	v_lshl_add_u32 v154, v154, 2, v196
	ds_add_u32 v154, v194
	s_mov_b64 exec, s[86:87]
	v_lshl_add_u32 v155, v155, 2, v196
	ds_add_u32 v155, v194
	s_mov_b64 exec, s[88:89]
	v_lshl_add_u32 v156, v156, 2, v196
	ds_add_u32 v156, v194
	s_mov_b64 exec, s[90:91]
	v_lshl_add_u32 v157, v157, 2, v196
	ds_add_u32 v157, v194
	s_mov_b64 exec, s[92:93]
	v_lshl_add_u32 v158, v158, 2, v196
	ds_add_u32 v158, v194
	s_mov_b64 exec, s[94:95]
	v_lshl_add_u32 v159, v159, 2, v196
	ds_add_u32 v159, v194
	s_mov_b64 exec, s[96:97]
	v_lshl_add_u32 v160, v160, 2, v196
	ds_add_u32 v160, v194
	s_mov_b64 exec, s[98:99]
	v_lshl_add_u32 v161, v161, 2, v196
	ds_add_u32 v161, v194
	s_mov_b64 exec, -1
	s_waitcnt lgkmcnt(0)
	s_barrier
	v_and_b32_e32 v228, 15, v0
	v_lshl_add_u32 v228, v228, 2, v196
	ds_read_b32 v229, v228
	v_fma_f32 v224, v62, v62, 0
	v_fmac_f32_e32 v224, v63, v63
	v_fmac_f32_e32 v224, v64, v64
	v_fmac_f32_e32 v224, v65, v65
	v_fmac_f32_e32 v224, v58, v58
	v_fmac_f32_e32 v224, v59, v59
	v_fmac_f32_e32 v224, v60, v60
	v_fmac_f32_e32 v224, v61, v61
	v_fmac_f32_e32 v224, v54, v54
	v_fmac_f32_e32 v224, v55, v55
	v_fmac_f32_e32 v224, v56, v56
	v_fmac_f32_e32 v224, v57, v57
	v_fmac_f32_e32 v224, v50, v50
	v_fmac_f32_e32 v224, v51, v51
	v_fmac_f32_e32 v224, v52, v52
	v_fmac_f32_e32 v224, v53, v53
	v_fmac_f32_e32 v224, v46, v46
	v_fmac_f32_e32 v224, v47, v47
	v_fmac_f32_e32 v224, v48, v48
	v_fmac_f32_e32 v224, v49, v49
	v_fmac_f32_e32 v224, v42, v42
	v_fmac_f32_e32 v224, v43, v43
	v_fmac_f32_e32 v224, v44, v44
	v_fmac_f32_e32 v224, v45, v45
	v_fmac_f32_e32 v224, v38, v38
	v_fmac_f32_e32 v224, v39, v39
	v_fmac_f32_e32 v224, v40, v40
	v_fmac_f32_e32 v224, v41, v41
	v_fmac_f32_e32 v224, v34, v34
	v_fmac_f32_e32 v224, v35, v35
	v_fmac_f32_e32 v224, v36, v36
	v_fmac_f32_e32 v224, v37, v37
	v_fmac_f32_e32 v224, v30, v30
	v_fmac_f32_e32 v224, v31, v31
	v_fmac_f32_e32 v224, v32, v32
	v_fmac_f32_e32 v224, v33, v33
	v_fmac_f32_e32 v224, v26, v26
	v_fmac_f32_e32 v224, v27, v27
	v_fmac_f32_e32 v224, v28, v28
	v_fmac_f32_e32 v224, v29, v29
	v_fmac_f32_e32 v224, v22, v22
	v_fmac_f32_e32 v224, v23, v23
	v_fmac_f32_e32 v224, v24, v24
	v_fmac_f32_e32 v224, v25, v25
	v_fmac_f32_e32 v224, v18, v18
	v_fmac_f32_e32 v224, v19, v19
	v_fmac_f32_e32 v224, v20, v20
	v_fmac_f32_e32 v224, v21, v21
	v_fmac_f32_e32 v224, v14, v14
	v_fmac_f32_e32 v224, v15, v15
	v_fmac_f32_e32 v224, v16, v16
	v_fmac_f32_e32 v224, v17, v17
	v_fmac_f32_e32 v224, v10, v10
	v_fmac_f32_e32 v224, v11, v11
	v_fmac_f32_e32 v224, v12, v12
	v_fmac_f32_e32 v224, v13, v13
	v_fmac_f32_e32 v224, v6, v6
	v_fmac_f32_e32 v224, v7, v7
	v_fmac_f32_e32 v224, v8, v8
	v_fmac_f32_e32 v224, v9, v9
	v_fmac_f32_e32 v224, v2, v2
	v_fmac_f32_e32 v224, v3, v3
	v_fmac_f32_e32 v224, v4, v4
	v_fmac_f32_e32 v224, v5, v5
	v_mbcnt_lo_u32_b32 v225, -1, 0
	v_mbcnt_hi_u32_b32 v225, -1, v225
	v_and_b32_e32 v227, 64, v225
	v_xor_b32_e32 v226, 16, v225
	v_add_u32_e32 v227, 64, v227
	v_cmp_lt_i32_e32 vcc, v226, v227
	s_nop 1
	v_cndmask_b32_e32 v226, v225, v226, vcc
	v_lshlrev_b32_e32 v226, 2, v226
	ds_bpermute_b32 v226, v226, v224
	s_waitcnt lgkmcnt(0)
	v_add_f32_e32 v224, v224, v226
	v_xor_b32_e32 v226, 32, v225
	v_cmp_lt_i32_e32 vcc, v226, v227
	s_nop 1
	v_cndmask_b32_e32 v225, v225, v226, vcc
	v_lshlrev_b32_e32 v225, 2, v225
	ds_bpermute_b32 v225, v225, v224
	v_mov_b32_e32 v230, v229
	s_nop 1
	v_add_u32_dpp v230, v230, v230 row_shr:1 row_mask:0xf bank_mask:0xf bound_ctrl:1
	s_nop 1
	v_add_u32_dpp v230, v230, v230 row_shr:2 row_mask:0xf bank_mask:0xf bound_ctrl:1
	s_nop 1
	v_add_u32_dpp v230, v230, v230 row_shr:4 row_mask:0xf bank_mask:0xf bound_ctrl:1
	s_nop 1
	v_add_u32_dpp v230, v230, v230 row_shr:8 row_mask:0xf bank_mask:0xf bound_ctrl:1
	s_nop 1
	v_sub_u32_e32 v231, v230, v229
	v_lshlrev_b32_e32 v231, 2, v231
	v_readlane_b32 s8, v230, 15
	v_cmp_gt_u32_e32 vcc, 16, v1
	s_and_saveexec_b64 s[30:31], vcc
	v_add_u32_e32 v226, s24, v1
	v_lshlrev_b32_e32 v226, 2, v226
	v_add_u32_e32 v226, 0x11300, v226
	s_waitcnt lgkmcnt(0)
	v_add_f32_e32 v224, v224, v225
	ds_write_b32 v226, v224
	s_cmp_lg_u32 s17, 0
	s_cbranch_scc1 .Lfront_nocursor
	ds_write_b32 v228, v231 offset:64
.Lfront_nocursor:
	s_mov_b64 exec, s[30:31]
	s_waitcnt lgkmcnt(0)
	s_barrier
	s_mov_b64 exec, s[36:37]
	ds_add_rtn_u32 v162, v130, v195 offset:64
	s_mov_b64 exec, s[38:39]
	ds_add_rtn_u32 v163, v131, v195 offset:64
	s_mov_b64 exec, s[40:41]
	ds_add_rtn_u32 v164, v132, v195 offset:64
	s_mov_b64 exec, s[42:43]
	ds_add_rtn_u32 v165, v133, v195 offset:64
	s_mov_b64 exec, s[44:45]
	ds_add_rtn_u32 v166, v134, v195 offset:64
	s_mov_b64 exec, s[46:47]
	ds_add_rtn_u32 v167, v135, v195 offset:64
	s_mov_b64 exec, s[48:49]
	ds_add_rtn_u32 v168, v136, v195 offset:64
	s_mov_b64 exec, s[50:51]
	ds_add_rtn_u32 v169, v137, v195 offset:64
	s_mov_b64 exec, s[52:53]
	ds_add_rtn_u32 v170, v138, v195 offset:64
	s_mov_b64 exec, s[54:55]
	ds_add_rtn_u32 v171, v139, v195 offset:64
	s_mov_b64 exec, s[56:57]
	ds_add_rtn_u32 v172, v140, v195 offset:64
	s_mov_b64 exec, s[58:59]
	ds_add_rtn_u32 v173, v141, v195 offset:64
	s_mov_b64 exec, s[60:61]
	ds_add_rtn_u32 v174, v142, v195 offset:64
	s_mov_b64 exec, s[62:63]
	ds_add_rtn_u32 v175, v143, v195 offset:64
	s_mov_b64 exec, s[64:65]
	ds_add_rtn_u32 v176, v144, v195 offset:64
	s_mov_b64 exec, s[66:67]
	ds_add_rtn_u32 v177, v145, v195 offset:64
	s_mov_b64 exec, s[68:69]
	ds_add_rtn_u32 v178, v146, v195 offset:64
	s_mov_b64 exec, s[70:71]
	ds_add_rtn_u32 v179, v147, v195 offset:64
	s_mov_b64 exec, s[72:73]
	ds_add_rtn_u32 v180, v148, v195 offset:64
	s_mov_b64 exec, s[74:75]
	ds_add_rtn_u32 v181, v149, v195 offset:64
	s_mov_b64 exec, s[76:77]
	ds_add_rtn_u32 v182, v150, v195 offset:64
	s_mov_b64 exec, s[78:79]
	ds_add_rtn_u32 v183, v151, v195 offset:64
	s_mov_b64 exec, s[80:81]
	ds_add_rtn_u32 v184, v152, v195 offset:64
	s_mov_b64 exec, s[82:83]
	ds_add_rtn_u32 v185, v153, v195 offset:64
	s_mov_b64 exec, s[84:85]
	ds_add_rtn_u32 v186, v154, v195 offset:64
	s_mov_b64 exec, s[86:87]
	ds_add_rtn_u32 v187, v155, v195 offset:64
	s_mov_b64 exec, s[88:89]
	ds_add_rtn_u32 v188, v156, v195 offset:64
	s_mov_b64 exec, s[90:91]
	ds_add_rtn_u32 v189, v157, v195 offset:64
	s_mov_b64 exec, s[92:93]
	ds_add_rtn_u32 v190, v158, v195 offset:64
	s_mov_b64 exec, s[94:95]
	ds_add_rtn_u32 v191, v159, v195 offset:64
	s_mov_b64 exec, s[96:97]
	ds_add_rtn_u32 v192, v160, v195 offset:64
	s_mov_b64 exec, s[98:99]
	ds_add_rtn_u32 v193, v161, v195 offset:64
	s_mov_b64 exec, -1
	v_add_u32_e32 v198, 0x0, v197
	v_and_or_b32 v198, v130, 60, v198
	s_waitcnt lgkmcnt(0)
	s_mov_b64 exec, s[36:37]
	ds_write_b32 v162, v198
	s_mov_b64 exec, -1
	v_add_u32_e32 v199, 0x40, v197
	v_and_or_b32 v199, v131, 60, v199
	s_mov_b64 exec, s[38:39]
	ds_write_b32 v163, v199
	s_mov_b64 exec, -1
	v_add_u32_e32 v198, 0x80, v197
	v_and_or_b32 v198, v132, 60, v198
	s_mov_b64 exec, s[40:41]
	ds_write_b32 v164, v198
	s_mov_b64 exec, -1
	v_add_u32_e32 v199, 0xc0, v197
	v_and_or_b32 v199, v133, 60, v199
	s_mov_b64 exec, s[42:43]
	ds_write_b32 v165, v199
	s_mov_b64 exec, -1
	v_add_u32_e32 v198, 0x10000, v197
	v_and_or_b32 v198, v134, 60, v198
	s_mov_b64 exec, s[44:45]
	ds_write_b32 v166, v198
	s_mov_b64 exec, -1
	v_add_u32_e32 v199, 0x10040, v197
	v_and_or_b32 v199, v135, 60, v199
	s_mov_b64 exec, s[46:47]
	ds_write_b32 v167, v199
	s_mov_b64 exec, -1
	v_add_u32_e32 v198, 0x10080, v197
	v_and_or_b32 v198, v136, 60, v198
	s_mov_b64 exec, s[48:49]
	ds_write_b32 v168, v198
	s_mov_b64 exec, -1
	v_add_u32_e32 v199, 0x100c0, v197
	v_and_or_b32 v199, v137, 60, v199
	s_mov_b64 exec, s[50:51]
	ds_write_b32 v169, v199
	s_mov_b64 exec, -1
	v_add_u32_e32 v198, 0x20000, v197
	v_and_or_b32 v198, v138, 60, v198
	s_mov_b64 exec, s[52:53]
	ds_write_b32 v170, v198
	s_mov_b64 exec, -1
	v_add_u32_e32 v199, 0x20040, v197
	v_and_or_b32 v199, v139, 60, v199
	s_mov_b64 exec, s[54:55]
	ds_write_b32 v171, v199
	s_mov_b64 exec, -1
	v_add_u32_e32 v198, 0x20080, v197
	v_and_or_b32 v198, v140, 60, v198
	s_mov_b64 exec, s[56:57]
	ds_write_b32 v172, v198
	s_mov_b64 exec, -1
	v_add_u32_e32 v199, 0x200c0, v197
	v_and_or_b32 v199, v141, 60, v199
	s_mov_b64 exec, s[58:59]
	ds_write_b32 v173, v199
	s_mov_b64 exec, -1
	v_add_u32_e32 v198, 0x30000, v197
	v_and_or_b32 v198, v142, 60, v198
	s_mov_b64 exec, s[60:61]
	ds_write_b32 v174, v198
	s_mov_b64 exec, -1
	v_add_u32_e32 v199, 0x30040, v197
	v_and_or_b32 v199, v143, 60, v199
	s_mov_b64 exec, s[62:63]
	ds_write_b32 v175, v199
	s_mov_b64 exec, -1
	v_add_u32_e32 v198, 0x30080, v197
	v_and_or_b32 v198, v144, 60, v198
	s_mov_b64 exec, s[64:65]
	ds_write_b32 v176, v198
	s_mov_b64 exec, -1
	v_add_u32_e32 v199, 0x300c0, v197
	v_and_or_b32 v199, v145, 60, v199
	s_mov_b64 exec, s[66:67]
	ds_write_b32 v177, v199
	s_mov_b64 exec, -1
	v_add_u32_e32 v198, 0x40000, v197
	v_and_or_b32 v198, v146, 60, v198
	s_mov_b64 exec, s[68:69]
	ds_write_b32 v178, v198
	s_mov_b64 exec, -1
	v_add_u32_e32 v199, 0x40040, v197
	v_and_or_b32 v199, v147, 60, v199
	s_mov_b64 exec, s[70:71]
	ds_write_b32 v179, v199
	s_mov_b64 exec, -1
	v_add_u32_e32 v198, 0x40080, v197
	v_and_or_b32 v198, v148, 60, v198
	s_mov_b64 exec, s[72:73]
	ds_write_b32 v180, v198
	s_mov_b64 exec, -1
	v_add_u32_e32 v199, 0x400c0, v197
	v_and_or_b32 v199, v149, 60, v199
	s_mov_b64 exec, s[74:75]
	ds_write_b32 v181, v199
	s_mov_b64 exec, -1
	v_add_u32_e32 v198, 0x50000, v197
	v_and_or_b32 v198, v150, 60, v198
	s_mov_b64 exec, s[76:77]
	ds_write_b32 v182, v198
	s_mov_b64 exec, -1
	v_add_u32_e32 v199, 0x50040, v197
	v_and_or_b32 v199, v151, 60, v199
	s_mov_b64 exec, s[78:79]
	ds_write_b32 v183, v199
	s_mov_b64 exec, -1
	v_add_u32_e32 v198, 0x50080, v197
	v_and_or_b32 v198, v152, 60, v198
	s_mov_b64 exec, s[80:81]
	ds_write_b32 v184, v198
	s_mov_b64 exec, -1
	v_add_u32_e32 v199, 0x500c0, v197
	v_and_or_b32 v199, v153, 60, v199
	s_mov_b64 exec, s[82:83]
	ds_write_b32 v185, v199
	s_mov_b64 exec, -1
	v_add_u32_e32 v198, 0x60000, v197
	v_and_or_b32 v198, v154, 60, v198
	s_mov_b64 exec, s[84:85]
	ds_write_b32 v186, v198
	s_mov_b64 exec, -1
	v_add_u32_e32 v199, 0x60040, v197
	v_and_or_b32 v199, v155, 60, v199
	s_mov_b64 exec, s[86:87]
	ds_write_b32 v187, v199
	s_mov_b64 exec, -1
	v_add_u32_e32 v198, 0x60080, v197
	v_and_or_b32 v198, v156, 60, v198
	s_mov_b64 exec, s[88:89]
	ds_write_b32 v188, v198
	s_mov_b64 exec, -1
	v_add_u32_e32 v199, 0x600c0, v197
	v_and_or_b32 v199, v157, 60, v199
	s_mov_b64 exec, s[90:91]
	ds_write_b32 v189, v199
	s_mov_b64 exec, -1
	v_add_u32_e32 v198, 0x70000, v197
	v_and_or_b32 v198, v158, 60, v198
	s_mov_b64 exec, s[92:93]
	ds_write_b32 v190, v198
	s_mov_b64 exec, -1
	v_add_u32_e32 v199, 0x70040, v197
	v_and_or_b32 v199, v159, 60, v199
	s_mov_b64 exec, s[94:95]
	ds_write_b32 v191, v199
	s_mov_b64 exec, -1
	v_add_u32_e32 v198, 0x70080, v197
	v_and_or_b32 v198, v160, 60, v198
	s_mov_b64 exec, s[96:97]
	ds_write_b32 v192, v198
	s_mov_b64 exec, -1
	v_add_u32_e32 v199, 0x700c0, v197
	v_and_or_b32 v199, v161, 60, v199
	s_mov_b64 exec, s[98:99]
	ds_write_b32 v193, v199
	s_mov_b64 exec, -1
	s_waitcnt lgkmcnt(0)
	s_barrier
	v_readlane_b32 s60, v232, 0
	v_readlane_b32 s61, v232, 1
	v_readlane_b32 s62, v232, 2
	v_readlane_b32 s63, v232, 3
	v_readlane_b32 s64, v232, 4
	v_readlane_b32 s65, v232, 5
	v_readlane_b32 s66, v232, 6
	v_readlane_b32 s67, v232, 7
	v_readlane_b32 s68, v232, 8
	v_readlane_b32 s69, v232, 9
	v_readlane_b32 s70, v232, 10
	v_readlane_b32 s71, v232, 11
	v_readlane_b32 s72, v232, 12
	v_readlane_b32 s73, v232, 13
	v_readlane_b32 s74, v232, 14
	v_readlane_b32 s75, v232, 15
	s_mul_i32 s37, s8, s17
	s_lshr_b32 s37, s37, 2
	s_add_i32 s38, s17, 1
	s_mul_i32 s38, s8, s38
	s_lshr_b32 s38, s38, 2
	v_mov_b32_e32 v200, 0
	v_mov_b32_e32 v201, 0
	v_mov_b32_e32 v202, 0
	v_mov_b32_e32 v203, 0
	v_mov_b32_e32 v204, 0
	v_mov_b32_e32 v205, 0
	v_mov_b32_e32 v206, 0
	v_mov_b32_e32 v207, 0
	s_mov_b32 s50, -1
	s_cmp_lt_u32 s37, s38
	s_cbranch_scc1 .Lg_block
	s_cmp_eq_u32 s9, 0
	s_cbranch_scc1 .Lg_alldone
.Lg_block:
	s_sub_u32 s39, s38, s37
	s_min_u32 s39, s39, 0x80
	s_add_u32 s39, s39, s9
	v_add_u32_e32 v221, s37, v1
	v_lshlrev_b32_e32 v221, 2, v221
	ds_read_b32 v216, v221
	ds_read_b32 v217, v221 offset:256
	s_waitcnt lgkmcnt(0)
	s_cmp_lg_u32 s50, -1
	s_cbranch_scc1 .Lg_havecur
	s_mov_b32 s50, s60
	s_cmp_lg_u32 s9, 0
	s_cbranch_scc1 .Lg_havecur
	v_readlane_b32 s50, v216, 0
	s_bfe_u32 s50, s50, 0x40002
.Lg_havecur:
	s_cmp_gt_u32 s39, 0
	s_cbranch_scc0 .Lg_prodone
	s_cmp_gt_u32 s9, 0
	s_cbranch_scc1 .Lg_pskip0
	s_sub_u32 s45, 0, s9
	s_and_b32 s46, s45, 63
	v_readlane_b32 s40, v216, s46
	v_readlane_b32 s47, v217, s46
	s_cmp_lt_u32 s45, 64
	s_cselect_b32 s40, s40, s47
	s_bfe_u32 s60, s40, 0x40002
	s_and_b32 s40, s40, 0xffffffc0
	s_lshl_b32 s40, s40, 4
	s_add_u32 s42, s32, s40
	s_addc_u32 s43, s33, 0
	global_load_dwordx4 v[66:69], v218, s[42:43] nt
.Lg_pskip0:
	s_cmp_gt_u32 s39, 1
	s_cbranch_scc0 .Lg_prodone
	s_cmp_gt_u32 s9, 1
	s_cbranch_scc1 .Lg_pskip1
	s_sub_u32 s45, 1, s9
	s_and_b32 s46, s45, 63
	v_readlane_b32 s40, v216, s46
	v_readlane_b32 s47, v217, s46
	s_cmp_lt_u32 s45, 64
	s_cselect_b32 s40, s40, s47
	s_bfe_u32 s61, s40, 0x40002
	s_and_b32 s40, s40, 0xffffffc0
	s_lshl_b32 s40, s40, 4
	s_add_u32 s42, s32, s40
	s_addc_u32 s43, s33, 0
	global_load_dwordx4 v[70:73], v218, s[42:43] nt
.Lg_pskip1:
	s_cmp_gt_u32 s39, 2
	s_cbranch_scc0 .Lg_prodone
	s_cmp_gt_u32 s9, 2
	s_cbranch_scc1 .Lg_pskip2
	s_sub_u32 s45, 2, s9
	s_and_b32 s46, s45, 63
	v_readlane_b32 s40, v216, s46
	v_readlane_b32 s47, v217, s46
	s_cmp_lt_u32 s45, 64
	s_cselect_b32 s40, s40, s47
	s_bfe_u32 s62, s40, 0x40002
	s_and_b32 s40, s40, 0xffffffc0
	s_lshl_b32 s40, s40, 4
	s_add_u32 s42, s32, s40
	s_addc_u32 s43, s33, 0
	global_load_dwordx4 v[74:77], v218, s[42:43] nt
.Lg_pskip2:
	s_cmp_gt_u32 s39, 3
	s_cbranch_scc0 .Lg_prodone
	s_cmp_gt_u32 s9, 3
	s_cbranch_scc1 .Lg_pskip3
	s_sub_u32 s45, 3, s9
	s_and_b32 s46, s45, 63
	v_readlane_b32 s40, v216, s46
	v_readlane_b32 s47, v217, s46
	s_cmp_lt_u32 s45, 64
	s_cselect_b32 s40, s40, s47
	s_bfe_u32 s63, s40, 0x40002
	s_and_b32 s40, s40, 0xffffffc0
	s_lshl_b32 s40, s40, 4
	s_add_u32 s42, s32, s40
	s_addc_u32 s43, s33, 0
	global_load_dwordx4 v[78:81], v218, s[42:43] nt
.Lg_pskip3:
	s_cmp_gt_u32 s39, 4
	s_cbranch_scc0 .Lg_prodone
	s_cmp_gt_u32 s9, 4
	s_cbranch_scc1 .Lg_pskip4
	s_sub_u32 s45, 4, s9
	s_and_b32 s46, s45, 63
	v_readlane_b32 s40, v216, s46
	v_readlane_b32 s47, v217, s46
	s_cmp_lt_u32 s45, 64
	s_cselect_b32 s40, s40, s47
	s_bfe_u32 s64, s40, 0x40002
	s_and_b32 s40, s40, 0xffffffc0
	s_lshl_b32 s40, s40, 4
	s_add_u32 s42, s32, s40
	s_addc_u32 s43, s33, 0
	global_load_dwordx4 v[82:85], v218, s[42:43] nt
.Lg_pskip4:
	s_cmp_gt_u32 s39, 5
	s_cbranch_scc0 .Lg_prodone
	s_cmp_gt_u32 s9, 5
	s_cbranch_scc1 .Lg_pskip5
	s_sub_u32 s45, 5, s9
	s_and_b32 s46, s45, 63
	v_readlane_b32 s40, v216, s46
	v_readlane_b32 s47, v217, s46
	s_cmp_lt_u32 s45, 64
	s_cselect_b32 s40, s40, s47
	s_bfe_u32 s65, s40, 0x40002
	s_and_b32 s40, s40, 0xffffffc0
	s_lshl_b32 s40, s40, 4
	s_add_u32 s42, s32, s40
	s_addc_u32 s43, s33, 0
	global_load_dwordx4 v[86:89], v218, s[42:43] nt
.Lg_pskip5:
	s_cmp_gt_u32 s39, 6
	s_cbranch_scc0 .Lg_prodone
	s_cmp_gt_u32 s9, 6
	s_cbranch_scc1 .Lg_pskip6
	s_sub_u32 s45, 6, s9
	s_and_b32 s46, s45, 63
	v_readlane_b32 s40, v216, s46
	v_readlane_b32 s47, v217, s46
	s_cmp_lt_u32 s45, 64
	s_cselect_b32 s40, s40, s47
	s_bfe_u32 s66, s40, 0x40002
	s_and_b32 s40, s40, 0xffffffc0
	s_lshl_b32 s40, s40, 4
	s_add_u32 s42, s32, s40
	s_addc_u32 s43, s33, 0
	global_load_dwordx4 v[90:93], v218, s[42:43] nt
.Lg_pskip6:
	s_cmp_gt_u32 s39, 7
	s_cbranch_scc0 .Lg_prodone
	s_cmp_gt_u32 s9, 7
	s_cbranch_scc1 .Lg_pskip7
	s_sub_u32 s45, 7, s9
	s_and_b32 s46, s45, 63
	v_readlane_b32 s40, v216, s46
	v_readlane_b32 s47, v217, s46
	s_cmp_lt_u32 s45, 64
	s_cselect_b32 s40, s40, s47
	s_bfe_u32 s67, s40, 0x40002
	s_and_b32 s40, s40, 0xffffffc0
	s_lshl_b32 s40, s40, 4
	s_add_u32 s42, s32, s40
	s_addc_u32 s43, s33, 0
	global_load_dwordx4 v[94:97], v218, s[42:43] nt
.Lg_pskip7:
	s_cmp_gt_u32 s39, 8
	s_cbranch_scc0 .Lg_prodone
	s_cmp_gt_u32 s9, 8
	s_cbranch_scc1 .Lg_pskip8
	s_sub_u32 s45, 8, s9
	s_and_b32 s46, s45, 63
	v_readlane_b32 s40, v216, s46
	v_readlane_b32 s47, v217, s46
	s_cmp_lt_u32 s45, 64
	s_cselect_b32 s40, s40, s47
	s_bfe_u32 s68, s40, 0x40002
	s_and_b32 s40, s40, 0xffffffc0
	s_lshl_b32 s40, s40, 4
	s_add_u32 s42, s32, s40
	s_addc_u32 s43, s33, 0
	global_load_dwordx4 v[98:101], v218, s[42:43] nt
.Lg_pskip8:
	s_cmp_gt_u32 s39, 9
	s_cbranch_scc0 .Lg_prodone
	s_cmp_gt_u32 s9, 9
	s_cbranch_scc1 .Lg_pskip9
	s_sub_u32 s45, 9, s9
	s_and_b32 s46, s45, 63
	v_readlane_b32 s40, v216, s46
	v_readlane_b32 s47, v217, s46
	s_cmp_lt_u32 s45, 64
	s_cselect_b32 s40, s40, s47
	s_bfe_u32 s69, s40, 0x40002
	s_and_b32 s40, s40, 0xffffffc0
	s_lshl_b32 s40, s40, 4
	s_add_u32 s42, s32, s40
	s_addc_u32 s43, s33, 0
	global_load_dwordx4 v[102:105], v218, s[42:43] nt
.Lg_pskip9:
	s_cmp_gt_u32 s39, 10
	s_cbranch_scc0 .Lg_prodone
	s_cmp_gt_u32 s9, 10
	s_cbranch_scc1 .Lg_pskip10
	s_sub_u32 s45, 10, s9
	s_and_b32 s46, s45, 63
	v_readlane_b32 s40, v216, s46
	v_readlane_b32 s47, v217, s46
	s_cmp_lt_u32 s45, 64
	s_cselect_b32 s40, s40, s47
	s_bfe_u32 s70, s40, 0x40002
	s_and_b32 s40, s40, 0xffffffc0
	s_lshl_b32 s40, s40, 4
	s_add_u32 s42, s32, s40
	s_addc_u32 s43, s33, 0
	global_load_dwordx4 v[106:109], v218, s[42:43] nt
.Lg_pskip10:
	s_cmp_gt_u32 s39, 11
	s_cbranch_scc0 .Lg_prodone
	s_cmp_gt_u32 s9, 11
	s_cbranch_scc1 .Lg_pskip11
	s_sub_u32 s45, 11, s9
	s_and_b32 s46, s45, 63
	v_readlane_b32 s40, v216, s46
	v_readlane_b32 s47, v217, s46
	s_cmp_lt_u32 s45, 64
	s_cselect_b32 s40, s40, s47
	s_bfe_u32 s71, s40, 0x40002
	s_and_b32 s40, s40, 0xffffffc0
	s_lshl_b32 s40, s40, 4
	s_add_u32 s42, s32, s40
	s_addc_u32 s43, s33, 0
	global_load_dwordx4 v[110:113], v218, s[42:43] nt
.Lg_pskip11:
	s_cmp_gt_u32 s39, 12
	s_cbranch_scc0 .Lg_prodone
	s_cmp_gt_u32 s9, 12
	s_cbranch_scc1 .Lg_pskip12
	s_sub_u32 s45, 12, s9
	s_and_b32 s46, s45, 63
	v_readlane_b32 s40, v216, s46
	v_readlane_b32 s47, v217, s46
	s_cmp_lt_u32 s45, 64
	s_cselect_b32 s40, s40, s47
	s_bfe_u32 s72, s40, 0x40002
	s_and_b32 s40, s40, 0xffffffc0
	s_lshl_b32 s40, s40, 4
	s_add_u32 s42, s32, s40
	s_addc_u32 s43, s33, 0
	global_load_dwordx4 v[114:117], v218, s[42:43] nt
.Lg_pskip12:
	s_cmp_gt_u32 s39, 13
	s_cbranch_scc0 .Lg_prodone
	s_cmp_gt_u32 s9, 13
	s_cbranch_scc1 .Lg_pskip13
	s_sub_u32 s45, 13, s9
	s_and_b32 s46, s45, 63
	v_readlane_b32 s40, v216, s46
	v_readlane_b32 s47, v217, s46
	s_cmp_lt_u32 s45, 64
	s_cselect_b32 s40, s40, s47
	s_bfe_u32 s73, s40, 0x40002
	s_and_b32 s40, s40, 0xffffffc0
	s_lshl_b32 s40, s40, 4
	s_add_u32 s42, s32, s40
	s_addc_u32 s43, s33, 0
	global_load_dwordx4 v[118:121], v218, s[42:43] nt
.Lg_pskip13:
	s_cmp_gt_u32 s39, 14
	s_cbranch_scc0 .Lg_prodone
	s_cmp_gt_u32 s9, 14
	s_cbranch_scc1 .Lg_pskip14
	s_sub_u32 s45, 14, s9
	s_and_b32 s46, s45, 63
	v_readlane_b32 s40, v216, s46
	v_readlane_b32 s47, v217, s46
	s_cmp_lt_u32 s45, 64
	s_cselect_b32 s40, s40, s47
	s_bfe_u32 s74, s40, 0x40002
	s_and_b32 s40, s40, 0xffffffc0
	s_lshl_b32 s40, s40, 4
	s_add_u32 s42, s32, s40
	s_addc_u32 s43, s33, 0
	global_load_dwordx4 v[122:125], v218, s[42:43] nt
.Lg_pskip14:
	s_cmp_gt_u32 s39, 15
	s_cbranch_scc0 .Lg_prodone
	s_cmp_gt_u32 s9, 15
	s_cbranch_scc1 .Lg_pskip15
	s_sub_u32 s45, 15, s9
	s_and_b32 s46, s45, 63
	v_readlane_b32 s40, v216, s46
	v_readlane_b32 s47, v217, s46
	s_cmp_lt_u32 s45, 64
	s_cselect_b32 s40, s40, s47
	s_bfe_u32 s75, s40, 0x40002
	s_and_b32 s40, s40, 0xffffffc0
	s_lshl_b32 s40, s40, 4
	s_add_u32 s42, s32, s40
	s_addc_u32 s43, s33, 0
	global_load_dwordx4 v[126:129], v218, s[42:43] nt
.Lg_pskip15:
.Lg_prodone:
	s_mov_b32 s44, 0
	s_cmp_ge_u32 s39, 16
	s_cbranch_scc1 .Lg_slot0
	s_waitcnt vmcnt(0)
.Lg_slot0:
	s_waitcnt vmcnt(15)
	s_cmp_lg_u32 s60, s50
	s_cbranch_scc1 .Lg_flush0
.Lg_cont0:
	v_cvt_f64_f32_e32 v[208:209], v66
	v_cvt_f64_f32_e32 v[210:211], v67
	v_cvt_f64_f32_e32 v[212:213], v68
	v_cvt_f64_f32_e32 v[214:215], v69
	v_add_f64 v[200:201], v[200:201], v[208:209]
	v_add_f64 v[202:203], v[202:203], v[210:211]
	v_add_f64 v[204:205], v[204:205], v[212:213]
	v_add_f64 v[206:207], v[206:207], v[214:215]
	s_add_u32 s41, s44, 16
	s_cmp_lt_u32 s41, s39
	s_cbranch_scc0 .Lg_tail0
	s_sub_u32 s45, s41, s9
	s_and_b32 s46, s45, 63
	v_readlane_b32 s40, v216, s46
	v_readlane_b32 s47, v217, s46
	s_cmp_lt_u32 s45, 64
	s_cselect_b32 s40, s40, s47
	s_bfe_u32 s60, s40, 0x40002
	s_and_b32 s40, s40, 0xffffffc0
	s_lshl_b32 s40, s40, 4
	s_add_u32 s42, s32, s40
	s_addc_u32 s43, s33, 0
	global_load_dwordx4 v[66:69], v218, s[42:43] nt

.Lg_slot1:
	s_waitcnt vmcnt(15)
	s_cmp_lg_u32 s61, s50
	s_cbranch_scc1 .Lg_flush1
.Lg_cont1:
	v_cvt_f64_f32_e32 v[208:209], v70
	v_cvt_f64_f32_e32 v[210:211], v71
	v_cvt_f64_f32_e32 v[212:213], v72
	v_cvt_f64_f32_e32 v[214:215], v73
	v_add_f64 v[200:201], v[200:201], v[208:209]
	v_add_f64 v[202:203], v[202:203], v[210:211]
	v_add_f64 v[204:205], v[204:205], v[212:213]
	v_add_f64 v[206:207], v[206:207], v[214:215]
	s_add_u32 s41, s44, 16
	s_cmp_lt_u32 s41, s39
	s_cbranch_scc0 .Lg_tail1
	s_sub_u32 s45, s41, s9
	s_and_b32 s46, s45, 63
	v_readlane_b32 s40, v216, s46
	v_readlane_b32 s47, v217, s46
	s_cmp_lt_u32 s45, 64
	s_cselect_b32 s40, s40, s47
	s_bfe_u32 s61, s40, 0x40002
	s_and_b32 s40, s40, 0xffffffc0
	s_lshl_b32 s40, s40, 4
	s_add_u32 s42, s32, s40
	s_addc_u32 s43, s33, 0
	global_load_dwordx4 v[70:73], v218, s[42:43] nt

.Lg_slot2:
	s_waitcnt vmcnt(15)
	s_cmp_lg_u32 s62, s50
	s_cbranch_scc1 .Lg_flush2
.Lg_cont2:
	v_cvt_f64_f32_e32 v[208:209], v74
	v_cvt_f64_f32_e32 v[210:211], v75
	v_cvt_f64_f32_e32 v[212:213], v76
	v_cvt_f64_f32_e32 v[214:215], v77
	v_add_f64 v[200:201], v[200:201], v[208:209]
	v_add_f64 v[202:203], v[202:203], v[210:211]
	v_add_f64 v[204:205], v[204:205], v[212:213]
	v_add_f64 v[206:207], v[206:207], v[214:215]
	s_add_u32 s41, s44, 16
	s_cmp_lt_u32 s41, s39
	s_cbranch_scc0 .Lg_tail2
	s_sub_u32 s45, s41, s9
	s_and_b32 s46, s45, 63
	v_readlane_b32 s40, v216, s46
	v_readlane_b32 s47, v217, s46
	s_cmp_lt_u32 s45, 64
	s_cselect_b32 s40, s40, s47
	s_bfe_u32 s62, s40, 0x40002
	s_and_b32 s40, s40, 0xffffffc0
	s_lshl_b32 s40, s40, 4
	s_add_u32 s42, s32, s40
	s_addc_u32 s43, s33, 0
	global_load_dwordx4 v[74:77], v218, s[42:43] nt

.Lg_slot3:
	s_waitcnt vmcnt(15)
	s_cmp_lg_u32 s63, s50
	s_cbranch_scc1 .Lg_flush3
.Lg_cont3:
	v_cvt_f64_f32_e32 v[208:209], v78
	v_cvt_f64_f32_e32 v[210:211], v79
	v_cvt_f64_f32_e32 v[212:213], v80
	v_cvt_f64_f32_e32 v[214:215], v81
	v_add_f64 v[200:201], v[200:201], v[208:209]
	v_add_f64 v[202:203], v[202:203], v[210:211]
	v_add_f64 v[204:205], v[204:205], v[212:213]
	v_add_f64 v[206:207], v[206:207], v[214:215]
	s_add_u32 s41, s44, 16
	s_cmp_lt_u32 s41, s39
	s_cbranch_scc0 .Lg_tail3
	s_sub_u32 s45, s41, s9
	s_and_b32 s46, s45, 63
	v_readlane_b32 s40, v216, s46
	v_readlane_b32 s47, v217, s46
	s_cmp_lt_u32 s45, 64
	s_cselect_b32 s40, s40, s47
	s_bfe_u32 s63, s40, 0x40002
	s_and_b32 s40, s40, 0xffffffc0
	s_lshl_b32 s40, s40, 4
	s_add_u32 s42, s32, s40
	s_addc_u32 s43, s33, 0
	global_load_dwordx4 v[78:81], v218, s[42:43] nt

.Lg_slot4:
	s_waitcnt vmcnt(15)
	s_cmp_lg_u32 s64, s50
	s_cbranch_scc1 .Lg_flush4
.Lg_cont4:
	v_cvt_f64_f32_e32 v[208:209], v82
	v_cvt_f64_f32_e32 v[210:211], v83
	v_cvt_f64_f32_e32 v[212:213], v84
	v_cvt_f64_f32_e32 v[214:215], v85
	v_add_f64 v[200:201], v[200:201], v[208:209]
	v_add_f64 v[202:203], v[202:203], v[210:211]
	v_add_f64 v[204:205], v[204:205], v[212:213]
	v_add_f64 v[206:207], v[206:207], v[214:215]
	s_add_u32 s41, s44, 16
	s_cmp_lt_u32 s41, s39
	s_cbranch_scc0 .Lg_tail4
	s_sub_u32 s45, s41, s9
	s_and_b32 s46, s45, 63
	v_readlane_b32 s40, v216, s46
	v_readlane_b32 s47, v217, s46
	s_cmp_lt_u32 s45, 64
	s_cselect_b32 s40, s40, s47
	s_bfe_u32 s64, s40, 0x40002
	s_and_b32 s40, s40, 0xffffffc0
	s_lshl_b32 s40, s40, 4
	s_add_u32 s42, s32, s40
	s_addc_u32 s43, s33, 0
	global_load_dwordx4 v[82:85], v218, s[42:43] nt

.Lg_slot5:
	s_waitcnt vmcnt(15)
	s_cmp_lg_u32 s65, s50
	s_cbranch_scc1 .Lg_flush5
.Lg_cont5:
	v_cvt_f64_f32_e32 v[208:209], v86
	v_cvt_f64_f32_e32 v[210:211], v87
	v_cvt_f64_f32_e32 v[212:213], v88
	v_cvt_f64_f32_e32 v[214:215], v89
	v_add_f64 v[200:201], v[200:201], v[208:209]
	v_add_f64 v[202:203], v[202:203], v[210:211]
	v_add_f64 v[204:205], v[204:205], v[212:213]
	v_add_f64 v[206:207], v[206:207], v[214:215]
	s_add_u32 s41, s44, 16
	s_cmp_lt_u32 s41, s39
	s_cbranch_scc0 .Lg_tail5
	s_sub_u32 s45, s41, s9
	s_and_b32 s46, s45, 63
	v_readlane_b32 s40, v216, s46
	v_readlane_b32 s47, v217, s46
	s_cmp_lt_u32 s45, 64
	s_cselect_b32 s40, s40, s47
	s_bfe_u32 s65, s40, 0x40002
	s_and_b32 s40, s40, 0xffffffc0
	s_lshl_b32 s40, s40, 4
	s_add_u32 s42, s32, s40
	s_addc_u32 s43, s33, 0
	global_load_dwordx4 v[86:89], v218, s[42:43] nt

.Lg_slot6:
	s_waitcnt vmcnt(15)
	s_cmp_lg_u32 s66, s50
	s_cbranch_scc1 .Lg_flush6
.Lg_cont6:
	v_cvt_f64_f32_e32 v[208:209], v90
	v_cvt_f64_f32_e32 v[210:211], v91
	v_cvt_f64_f32_e32 v[212:213], v92
	v_cvt_f64_f32_e32 v[214:215], v93
	v_add_f64 v[200:201], v[200:201], v[208:209]
	v_add_f64 v[202:203], v[202:203], v[210:211]
	v_add_f64 v[204:205], v[204:205], v[212:213]
	v_add_f64 v[206:207], v[206:207], v[214:215]
	s_add_u32 s41, s44, 16
	s_cmp_lt_u32 s41, s39
	s_cbranch_scc0 .Lg_tail6
	s_sub_u32 s45, s41, s9
	s_and_b32 s46, s45, 63
	v_readlane_b32 s40, v216, s46
	v_readlane_b32 s47, v217, s46
	s_cmp_lt_u32 s45, 64
	s_cselect_b32 s40, s40, s47
	s_bfe_u32 s66, s40, 0x40002
	s_and_b32 s40, s40, 0xffffffc0
	s_lshl_b32 s40, s40, 4
	s_add_u32 s42, s32, s40
	s_addc_u32 s43, s33, 0
	global_load_dwordx4 v[90:93], v218, s[42:43] nt

.Lg_slot7:
	s_waitcnt vmcnt(15)
	s_cmp_lg_u32 s67, s50
	s_cbranch_scc1 .Lg_flush7
.Lg_cont7:
	v_cvt_f64_f32_e32 v[208:209], v94
	v_cvt_f64_f32_e32 v[210:211], v95
	v_cvt_f64_f32_e32 v[212:213], v96
	v_cvt_f64_f32_e32 v[214:215], v97
	v_add_f64 v[200:201], v[200:201], v[208:209]
	v_add_f64 v[202:203], v[202:203], v[210:211]
	v_add_f64 v[204:205], v[204:205], v[212:213]
	v_add_f64 v[206:207], v[206:207], v[214:215]
	s_add_u32 s41, s44, 16
	s_cmp_lt_u32 s41, s39
	s_cbranch_scc0 .Lg_tail7
	s_sub_u32 s45, s41, s9
	s_and_b32 s46, s45, 63
	v_readlane_b32 s40, v216, s46
	v_readlane_b32 s47, v217, s46
	s_cmp_lt_u32 s45, 64
	s_cselect_b32 s40, s40, s47
	s_bfe_u32 s67, s40, 0x40002
	s_and_b32 s40, s40, 0xffffffc0
	s_lshl_b32 s40, s40, 4
	s_add_u32 s42, s32, s40
	s_addc_u32 s43, s33, 0
	global_load_dwordx4 v[94:97], v218, s[42:43] nt

.Lg_slot8:
	s_waitcnt vmcnt(15)
	s_cmp_lg_u32 s68, s50
	s_cbranch_scc1 .Lg_flush8
.Lg_cont8:
	v_cvt_f64_f32_e32 v[208:209], v98
	v_cvt_f64_f32_e32 v[210:211], v99
	v_cvt_f64_f32_e32 v[212:213], v100
	v_cvt_f64_f32_e32 v[214:215], v101
	v_add_f64 v[200:201], v[200:201], v[208:209]
	v_add_f64 v[202:203], v[202:203], v[210:211]
	v_add_f64 v[204:205], v[204:205], v[212:213]
	v_add_f64 v[206:207], v[206:207], v[214:215]
	s_add_u32 s41, s44, 16
	s_cmp_lt_u32 s41, s39
	s_cbranch_scc0 .Lg_tail8
	s_sub_u32 s45, s41, s9
	s_and_b32 s46, s45, 63
	v_readlane_b32 s40, v216, s46
	v_readlane_b32 s47, v217, s46
	s_cmp_lt_u32 s45, 64
	s_cselect_b32 s40, s40, s47
	s_bfe_u32 s68, s40, 0x40002
	s_and_b32 s40, s40, 0xffffffc0
	s_lshl_b32 s40, s40, 4
	s_add_u32 s42, s32, s40
	s_addc_u32 s43, s33, 0
	global_load_dwordx4 v[98:101], v218, s[42:43] nt

.Lg_slot9:
	s_waitcnt vmcnt(15)
	s_cmp_lg_u32 s69, s50
	s_cbranch_scc1 .Lg_flush9
.Lg_cont9:
	v_cvt_f64_f32_e32 v[208:209], v102
	v_cvt_f64_f32_e32 v[210:211], v103
	v_cvt_f64_f32_e32 v[212:213], v104
	v_cvt_f64_f32_e32 v[214:215], v105
	v_add_f64 v[200:201], v[200:201], v[208:209]
	v_add_f64 v[202:203], v[202:203], v[210:211]
	v_add_f64 v[204:205], v[204:205], v[212:213]
	v_add_f64 v[206:207], v[206:207], v[214:215]
	s_add_u32 s41, s44, 16
	s_cmp_lt_u32 s41, s39
	s_cbranch_scc0 .Lg_tail9
	s_sub_u32 s45, s41, s9
	s_and_b32 s46, s45, 63
	v_readlane_b32 s40, v216, s46
	v_readlane_b32 s47, v217, s46
	s_cmp_lt_u32 s45, 64
	s_cselect_b32 s40, s40, s47
	s_bfe_u32 s69, s40, 0x40002
	s_and_b32 s40, s40, 0xffffffc0
	s_lshl_b32 s40, s40, 4
	s_add_u32 s42, s32, s40
	s_addc_u32 s43, s33, 0
	global_load_dwordx4 v[102:105], v218, s[42:43] nt

.Lg_slot10:
	s_waitcnt vmcnt(15)
	s_cmp_lg_u32 s70, s50
	s_cbranch_scc1 .Lg_flush10
.Lg_cont10:
	v_cvt_f64_f32_e32 v[208:209], v106
	v_cvt_f64_f32_e32 v[210:211], v107
	v_cvt_f64_f32_e32 v[212:213], v108
	v_cvt_f64_f32_e32 v[214:215], v109
	v_add_f64 v[200:201], v[200:201], v[208:209]
	v_add_f64 v[202:203], v[202:203], v[210:211]
	v_add_f64 v[204:205], v[204:205], v[212:213]
	v_add_f64 v[206:207], v[206:207], v[214:215]
	s_add_u32 s41, s44, 16
	s_cmp_lt_u32 s41, s39
	s_cbranch_scc0 .Lg_tail10
	s_sub_u32 s45, s41, s9
	s_and_b32 s46, s45, 63
	v_readlane_b32 s40, v216, s46
	v_readlane_b32 s47, v217, s46
	s_cmp_lt_u32 s45, 64
	s_cselect_b32 s40, s40, s47
	s_bfe_u32 s70, s40, 0x40002
	s_and_b32 s40, s40, 0xffffffc0
	s_lshl_b32 s40, s40, 4
	s_add_u32 s42, s32, s40
	s_addc_u32 s43, s33, 0
	global_load_dwordx4 v[106:109], v218, s[42:43] nt

.Lg_slot11:
	s_waitcnt vmcnt(15)
	s_cmp_lg_u32 s71, s50
	s_cbranch_scc1 .Lg_flush11
.Lg_cont11:
	v_cvt_f64_f32_e32 v[208:209], v110
	v_cvt_f64_f32_e32 v[210:211], v111
	v_cvt_f64_f32_e32 v[212:213], v112
	v_cvt_f64_f32_e32 v[214:215], v113
	v_add_f64 v[200:201], v[200:201], v[208:209]
	v_add_f64 v[202:203], v[202:203], v[210:211]
	v_add_f64 v[204:205], v[204:205], v[212:213]
	v_add_f64 v[206:207], v[206:207], v[214:215]
	s_add_u32 s41, s44, 16
	s_cmp_lt_u32 s41, s39
	s_cbranch_scc0 .Lg_tail11
	s_sub_u32 s45, s41, s9
	s_and_b32 s46, s45, 63
	v_readlane_b32 s40, v216, s46
	v_readlane_b32 s47, v217, s46
	s_cmp_lt_u32 s45, 64
	s_cselect_b32 s40, s40, s47
	s_bfe_u32 s71, s40, 0x40002
	s_and_b32 s40, s40, 0xffffffc0
	s_lshl_b32 s40, s40, 4
	s_add_u32 s42, s32, s40
	s_addc_u32 s43, s33, 0
	global_load_dwordx4 v[110:113], v218, s[42:43] nt

.Lg_slot12:
	s_waitcnt vmcnt(15)
	s_cmp_lg_u32 s72, s50
	s_cbranch_scc1 .Lg_flush12
.Lg_cont12:
	v_cvt_f64_f32_e32 v[208:209], v114
	v_cvt_f64_f32_e32 v[210:211], v115
	v_cvt_f64_f32_e32 v[212:213], v116
	v_cvt_f64_f32_e32 v[214:215], v117
	v_add_f64 v[200:201], v[200:201], v[208:209]
	v_add_f64 v[202:203], v[202:203], v[210:211]
	v_add_f64 v[204:205], v[204:205], v[212:213]
	v_add_f64 v[206:207], v[206:207], v[214:215]
	s_add_u32 s41, s44, 16
	s_cmp_lt_u32 s41, s39
	s_cbranch_scc0 .Lg_tail12
	s_sub_u32 s45, s41, s9
	s_and_b32 s46, s45, 63
	v_readlane_b32 s40, v216, s46
	v_readlane_b32 s47, v217, s46
	s_cmp_lt_u32 s45, 64
	s_cselect_b32 s40, s40, s47
	s_bfe_u32 s72, s40, 0x40002
	s_and_b32 s40, s40, 0xffffffc0
	s_lshl_b32 s40, s40, 4
	s_add_u32 s42, s32, s40
	s_addc_u32 s43, s33, 0
	global_load_dwordx4 v[114:117], v218, s[42:43] nt

.Lg_slot13:
	s_waitcnt vmcnt(15)
	s_cmp_lg_u32 s73, s50
	s_cbranch_scc1 .Lg_flush13
.Lg_cont13:
	v_cvt_f64_f32_e32 v[208:209], v118
	v_cvt_f64_f32_e32 v[210:211], v119
	v_cvt_f64_f32_e32 v[212:213], v120
	v_cvt_f64_f32_e32 v[214:215], v121
	v_add_f64 v[200:201], v[200:201], v[208:209]
	v_add_f64 v[202:203], v[202:203], v[210:211]
	v_add_f64 v[204:205], v[204:205], v[212:213]
	v_add_f64 v[206:207], v[206:207], v[214:215]
	s_add_u32 s41, s44, 16
	s_cmp_lt_u32 s41, s39
	s_cbranch_scc0 .Lg_tail13
	s_sub_u32 s45, s41, s9
	s_and_b32 s46, s45, 63
	v_readlane_b32 s40, v216, s46
	v_readlane_b32 s47, v217, s46
	s_cmp_lt_u32 s45, 64
	s_cselect_b32 s40, s40, s47
	s_bfe_u32 s73, s40, 0x40002
	s_and_b32 s40, s40, 0xffffffc0
	s_lshl_b32 s40, s40, 4
	s_add_u32 s42, s32, s40
	s_addc_u32 s43, s33, 0
	global_load_dwordx4 v[118:121], v218, s[42:43] nt

.Lg_slot14:
	s_waitcnt vmcnt(15)
	s_cmp_lg_u32 s74, s50
	s_cbranch_scc1 .Lg_flush14
.Lg_cont14:
	v_cvt_f64_f32_e32 v[208:209], v122
	v_cvt_f64_f32_e32 v[210:211], v123
	v_cvt_f64_f32_e32 v[212:213], v124
	v_cvt_f64_f32_e32 v[214:215], v125
	v_add_f64 v[200:201], v[200:201], v[208:209]
	v_add_f64 v[202:203], v[202:203], v[210:211]
	v_add_f64 v[204:205], v[204:205], v[212:213]
	v_add_f64 v[206:207], v[206:207], v[214:215]
	s_add_u32 s41, s44, 16
	s_cmp_lt_u32 s41, s39
	s_cbranch_scc0 .Lg_tail14
	s_sub_u32 s45, s41, s9
	s_and_b32 s46, s45, 63
	v_readlane_b32 s40, v216, s46
	v_readlane_b32 s47, v217, s46
	s_cmp_lt_u32 s45, 64
	s_cselect_b32 s40, s40, s47
	s_bfe_u32 s74, s40, 0x40002
	s_and_b32 s40, s40, 0xffffffc0
	s_lshl_b32 s40, s40, 4
	s_add_u32 s42, s32, s40
	s_addc_u32 s43, s33, 0
	global_load_dwordx4 v[122:125], v218, s[42:43] nt

.Lg_slot15:
	s_waitcnt vmcnt(15)
	s_cmp_lg_u32 s75, s50
	s_cbranch_scc1 .Lg_flush15
.Lg_cont15:
	v_cvt_f64_f32_e32 v[208:209], v126
	v_cvt_f64_f32_e32 v[210:211], v127
	v_cvt_f64_f32_e32 v[212:213], v128
	v_cvt_f64_f32_e32 v[214:215], v129
	v_add_f64 v[200:201], v[200:201], v[208:209]
	v_add_f64 v[202:203], v[202:203], v[210:211]
	v_add_f64 v[204:205], v[204:205], v[212:213]
	v_add_f64 v[206:207], v[206:207], v[214:215]
	s_add_u32 s41, s44, 16
	s_cmp_lt_u32 s41, s39
	s_cbranch_scc0 .Lg_tail15
	s_sub_u32 s45, s41, s9
	s_and_b32 s46, s45, 63
	v_readlane_b32 s40, v216, s46
	v_readlane_b32 s47, v217, s46
	s_cmp_lt_u32 s45, 64
	s_cselect_b32 s40, s40, s47
	s_bfe_u32 s75, s40, 0x40002
	s_and_b32 s40, s40, 0xffffffc0
	s_lshl_b32 s40, s40, 4
	s_add_u32 s42, s32, s40
	s_addc_u32 s43, s33, 0
	global_load_dwordx4 v[126:129], v218, s[42:43] nt

.Lg_blockdone:
	s_sub_u32 s45, s39, s9
	s_add_u32 s37, s37, s45
	s_mov_b32 s9, 0
	s_cmp_lt_u32 s37, s38
	s_cbranch_scc1 .Lg_block
	s_mul_i32 s42, s50, 0x810
	v_add_u32_e32 v220, s42, v219
	ds_add_f64 v220, v[200:201] offset:32768
	ds_add_f64 v220, v[202:203] offset:33280
	ds_add_f64 v220, v[204:205] offset:33792
	ds_add_f64 v220, v[206:207] offset:34304
.Lg_alldone:
	s_cmp_lg_u32 s17, 0
	s_cbranch_scc1 .Lg_nofix
	v_cmp_gt_u32_e32 vcc, 16, v1
	s_and_saveexec_b64 s[30:31], vcc
	v_lshl_add_u32 v228, v1, 2, v196
	ds_read_b32 v229, v228
	ds_read_b32 v230, v228 offset:1024
	s_waitcnt lgkmcnt(0)
	v_add_u32_e32 v229, v229, v230
	ds_write_b32 v228, v229
	s_mov_b64 exec, s[30:31]

	.amdhsa_kernel _Z7vq_mainPKfPKiS0_PfPhPdPi
		.amdhsa_group_segment_fixed_size 71936
		.amdhsa_private_segment_fixed_size 0
		.amdhsa_kernarg_size 56
		.amdhsa_user_sgpr_count 2
		.amdhsa_user_sgpr_dispatch_ptr 0
		.amdhsa_user_sgpr_queue_ptr 0
		.amdhsa_user_sgpr_kernarg_segment_ptr 1
		.amdhsa_user_sgpr_dispatch_id 0
		.amdhsa_user_sgpr_kernarg_preload_length 0
		.amdhsa_user_sgpr_kernarg_preload_offset 0
		.amdhsa_user_sgpr_private_segment_size 0
		.amdhsa_uses_dynamic_stack 0
		.amdhsa_enable_private_segment 0
		.amdhsa_system_sgpr_workgroup_id_x 1
		.amdhsa_system_sgpr_workgroup_id_y 0
		.amdhsa_system_sgpr_workgroup_id_z 0
		.amdhsa_system_sgpr_workgroup_info 0
		.amdhsa_system_vgpr_workitem_id 0
		.amdhsa_next_free_vgpr 240
		.amdhsa_next_free_sgpr 102
		.amdhsa_accum_offset 236
		.amdhsa_reserve_vcc 1
		.amdhsa_float_round_mode_32 0
		.amdhsa_float_round_mode_16_64 0
		.amdhsa_float_denorm_mode_32 3
		.amdhsa_float_denorm_mode_16_64 3
		.amdhsa_dx10_clamp 1
		.amdhsa_ieee_mode 1
		.amdhsa_fp16_overflow 0
		.amdhsa_tg_split 0
		.amdhsa_exception_fp_ieee_invalid_op 0
		.amdhsa_exception_fp_denorm_src 0
		.amdhsa_exception_fp_ieee_div_zero 0
		.amdhsa_exception_fp_ieee_overflow 0
		.amdhsa_exception_fp_ieee_underflow 0
		.amdhsa_exception_fp_ieee_inexact 0
		.amdhsa_exception_int_div_zero 0
	.end_amdhsa_kernel

_Z11vq_finalizePK15HIP_vector_typeIjLj4EEPKdPKiPf:
	s_load_dwordx8 s[16:23], s[0:1], 0x0
	v_lshlrev_b32_e32 v1, 5, v0
	v_mov_b64_e32 v[10:11], 0
	v_mov_b32_e32 v12, 0
	s_waitcnt lgkmcnt(0)
	global_load_dwordx4 v[2:5], v1, s[16:17] offset:16
	global_load_dwordx4 v[6:9], v1, s[16:17]
	s_movk_i32 s2, 0x200
	v_cmp_gt_u32_e32 vcc, s2, v0
	s_and_saveexec_b64 s[2:3], vcc
	s_cbranch_execz .LBB1_2
	v_lshlrev_b32_e32 v13, 3, v0
	v_lshlrev_b32_e32 v1, 2, v0
	s_waitcnt lgkmcnt(0)
	global_load_dwordx2 v[10:11], v13, s[18:19]
	global_load_dword v12, v1, s[20:21]

.LBB1_7:
	s_or_b64 exec, exec, s[2:3]
	v_cmp_gt_u32_e32 vcc, 64, v0
	s_waitcnt lgkmcnt(0)
	s_barrier
	s_and_saveexec_b64 s[2:3], vcc
	s_cbranch_execz .LBB1_10
	v_lshlrev_b32_e32 v0, 2, v1
	ds_read_b32 v0, v0
	v_mov_b32_e32 v2, 0x2edbe6ff
	s_mov_b32 s2, 0x800000
	s_mov_b32 s3, 0x7f800000
	s_waitcnt lgkmcnt(0)
	v_fmac_f32_e32 v2, 0x39000000, v0
	v_cmp_gt_f32_e32 vcc, s2, v2
	s_mov_b32 s2, 0x3f317217
	v_mul_f32_e32 v0, 0x39000000, v0
	v_cndmask_b32_e64 v3, 0, 32, vcc
	v_ldexp_f32 v2, v2, v3
	v_log_f32_e32 v2, v2
	s_nop 0
	v_mul_f32_e32 v3, 0x3f317217, v2
	v_fma_f32 v3, v2, s2, -v3
	v_fmamk_f32 v3, v2, 0x3377d1cf, v3
	v_fmac_f32_e32 v3, 0x3f317217, v2
	v_cmp_lt_f32_e64 s[2:3], |v2|, s3
	s_nop 1
	v_cndmask_b32_e64 v2, v2, v3, s[2:3]
	v_mov_b32_e32 v3, 0x41b17218
	v_cndmask_b32_e32 v3, 0, v3, vcc
	v_sub_f32_e32 v2, v2, v3
	v_mul_f32_e32 v3, v0, v2
	v_cmp_eq_u32_e32 vcc, 0, v1
	s_nop 0
	v_mov_b32_dpp v3, v3 quad_perm:[1,0,3,2] row_mask:0xf bank_mask:0xf bound_ctrl:1
	v_fmac_f32_e32 v3, v0, v2
	s_nop 1
	v_add_f32_dpp v0, v3, v3 quad_perm:[2,3,0,1] row_mask:0xf bank_mask:0xf bound_ctrl:1
	s_nop 1
	v_add_f32_dpp v0, v0, v0 row_half_mirror row_mask:0xf bank_mask:0xf bound_ctrl:1
	s_nop 1
	v_add_f32_dpp v0, v0, v0 row_mirror row_mask:0xf bank_mask:0xf bound_ctrl:1
	s_nop 0
	v_readlane_b32 s4, v0, 0
	v_readlane_b32 s5, v0, 16
	v_readlane_b32 s2, v0, 32
	v_readlane_b32 s3, v0, 48
	s_and_b64 exec, exec, vcc
	s_cbranch_execz .LBB1_10
	v_mov_b32_e32 v0, s5
	v_mov_b32_e32 v23, 0
	v_add_f32_e32 v22, s4, v0
	ds_read_b128 v[0:3], v23 offset:256
	ds_read_b128 v[4:7], v23 offset:272
	ds_read_b128 v[8:11], v23 offset:320
	ds_read_b128 v[12:15], v23 offset:288
	ds_read_b128 v[16:19], v23 offset:304
	s_waitcnt lgkmcnt(4)
	v_add_f64 v[0:1], v[0:1], 0
	v_add_f64 v[20:21], v[0:1], v[2:3]
	ds_read_b128 v[0:3], v23 offset:336
	s_waitcnt lgkmcnt(3)
	v_add_u32_e32 v8, v9, v8
	v_add_f64 v[4:5], v[20:21], v[4:5]
	v_add_u32_e32 v8, v10, v8
	v_add_f64 v[4:5], v[4:5], v[6:7]
	v_add_u32_e32 v6, v11, v8
	s_waitcnt lgkmcnt(2)
	v_add_f64 v[4:5], v[4:5], v[12:13]
	s_waitcnt lgkmcnt(0)
	v_add_u32_e32 v0, v0, v6
	v_add_f64 v[4:5], v[4:5], v[14:15]
	v_add_u32_e32 v6, v1, v0
	v_add_f64 v[0:1], v[4:5], v[16:17]
	v_add_u32_e32 v2, v2, v6
	v_add_f64 v[0:1], v[0:1], v[18:19]
	v_add_u32_e32 v2, v3, v2
	v_ldexp_f64 v[0:1], v[0:1], -2
	v_cvt_f64_i32_e32 v[2:3], v2
	v_div_scale_f64 v[4:5], s[4:5], v[2:3], v[2:3], v[0:1]
	v_rcp_f64_e32 v[6:7], v[4:5]
	v_mov_b32_e32 v8, s3
	v_add_f32_e32 v8, s2, v8
	v_add_f32_e32 v12, v22, v8
	v_fma_f64 v[8:9], -v[4:5], v[6:7], 1.0
	v_fmac_f64_e32 v[6:7], v[6:7], v[8:9]
	v_fma_f64 v[8:9], -v[4:5], v[6:7], 1.0
	v_fmac_f64_e32 v[6:7], v[6:7], v[8:9]
	v_div_scale_f64 v[8:9], vcc, v[0:1], v[2:3], v[0:1]
	v_mul_f64 v[10:11], v[8:9], v[6:7]
	v_fma_f64 v[4:5], -v[4:5], v[10:11], v[8:9]
	s_mov_b32 s2, 0xbfb8aa3b
	v_mul_f32_e32 v8, 0xbfb8aa3b, v12
	v_fma_f32 v9, v12, s2, -v8
	v_rndne_f32_e32 v13, v8
	v_fmamk_f32 v9, v12, 0xb2a5705f, v9
	v_sub_f32_e32 v8, v8, v13
	v_add_f32_e32 v8, v8, v9
	v_exp_f32_e32 v8, v8
	v_cvt_i32_f32_e32 v9, v13
	v_div_fmas_f64 v[4:5], v[4:5], v[6:7], v[10:11]
	v_div_fixup_f64 v[0:1], v[4:5], v[2:3], v[0:1]
	s_mov_b32 s2, 0x42ce8ed0
	v_cvt_f32_f64_e32 v0, v[0:1]
	v_ldexp_f32 v1, v8, v9
	v_cmp_nlt_f32_e32 vcc, s2, v12
	s_mov_b32 s2, 0xc2b17218
	v_mov_b32_e32 v2, 0x7f800000
	v_cndmask_b32_e32 v1, 0, v1, vcc
	v_cmp_ngt_f32_e32 vcc, s2, v12
	s_nop 1
	v_cndmask_b32_e32 v1, v2, v1, vcc
	v_mov_b32_e32 v2, 0x800000
	s_waitcnt lgkmcnt(0)
	global_store_dwordx2 v2, v[0:1], s[22:23]

	.amdhsa_kernel _Z11vq_finalizePK15HIP_vector_typeIjLj4EEPKdPKiPf
		.amdhsa_group_segment_fixed_size 352
		.amdhsa_private_segment_fixed_size 0
		.amdhsa_kernarg_size 32
		.amdhsa_user_sgpr_count 2
		.amdhsa_user_sgpr_dispatch_ptr 0
		.amdhsa_user_sgpr_queue_ptr 0
		.amdhsa_user_sgpr_kernarg_segment_ptr 1
		.amdhsa_user_sgpr_dispatch_id 0
		.amdhsa_user_sgpr_kernarg_preload_length 0
		.amdhsa_user_sgpr_kernarg_preload_offset 0
		.amdhsa_user_sgpr_private_segment_size 0
		.amdhsa_uses_dynamic_stack 0
		.amdhsa_enable_private_segment 0
		.amdhsa_system_sgpr_workgroup_id_x 1
		.amdhsa_system_sgpr_workgroup_id_y 0
		.amdhsa_system_sgpr_workgroup_id_z 0
		.amdhsa_system_sgpr_workgroup_info 0
		.amdhsa_system_vgpr_workitem_id 0
		.amdhsa_next_free_vgpr 24
		.amdhsa_next_free_sgpr 24
		.amdhsa_accum_offset 24
		.amdhsa_reserve_vcc 1
		.amdhsa_float_round_mode_32 0
		.amdhsa_float_round_mode_16_64 0
		.amdhsa_float_denorm_mode_32 3
		.amdhsa_float_denorm_mode_16_64 3
		.amdhsa_dx10_clamp 1
		.amdhsa_ieee_mode 1
		.amdhsa_fp16_overflow 0
		.amdhsa_tg_split 0
		.amdhsa_exception_fp_ieee_invalid_op 0
		.amdhsa_exception_fp_denorm_src 0
		.amdhsa_exception_fp_ieee_div_zero 0
		.amdhsa_exception_fp_ieee_overflow 0
		.amdhsa_exception_fp_ieee_underflow 0
		.amdhsa_exception_fp_ieee_inexact 0
		.amdhsa_exception_int_div_zero 0
	.end_amdhsa_kernel

amdhsa.kernels:
  - .agpr_count:     4
    .args:
      - .actual_access:  read_only
        .address_space:  global
        .offset:         0
        .size:           8
        .value_kind:     global_buffer
      - .actual_access:  read_only
        .address_space:  global
        .offset:         8
        .size:           8
        .value_kind:     global_buffer
      - .actual_access:  read_only
        .address_space:  global
        .offset:         16
        .size:           8
        .value_kind:     global_buffer
      - .actual_access:  write_only
        .address_space:  global
        .offset:         24
        .size:           8
        .value_kind:     global_buffer
      - .actual_access:  write_only
        .address_space:  global
        .offset:         32
        .size:           8
        .value_kind:     global_buffer
      - .actual_access:  write_only
        .address_space:  global
        .offset:         40
        .size:           8
        .value_kind:     global_buffer
      - .actual_access:  write_only
        .address_space:  global
        .offset:         48
        .size:           8
        .value_kind:     global_buffer
    .group_segment_fixed_size: 71936
    .kernarg_segment_align: 8
    .kernarg_segment_size: 56
    .language:       OpenCL C
    .language_version:
      - 2
      - 0
    .max_flat_workgroup_size: 256
    .name:           _Z7vq_mainPKfPKiS0_PfPhPdPi
    .private_segment_fixed_size: 0
    .sgpr_count:     108
    .sgpr_spill_count: 0
    .symbol:         _Z7vq_mainPKfPKiS0_PfPhPdPi.kd
    .uniform_work_group_size: 1
    .uses_dynamic_stack: false
    .vgpr_count:     240
    .vgpr_spill_count: 0
    .wavefront_size: 64
  - .agpr_count:     0
    .args:
      - .actual_access:  read_only
        .address_space:  global
        .offset:         0
        .size:           8
        .value_kind:     global_buffer
      - .actual_access:  read_only
        .address_space:  global
        .offset:         8
        .size:           8
        .value_kind:     global_buffer
      - .actual_access:  read_only
        .address_space:  global
        .offset:         16
        .size:           8
        .value_kind:     global_buffer
      - .actual_access:  write_only
        .address_space:  global
        .offset:         24
        .size:           8
        .value_kind:     global_buffer
    .group_segment_fixed_size: 352
    .kernarg_segment_align: 8
    .kernarg_segment_size: 32
    .language:       OpenCL C
    .language_version:
      - 2
      - 0
    .max_flat_workgroup_size: 1024
    .name:           _Z11vq_finalizePK15HIP_vector_typeIjLj4EEPKdPKiPf
    .private_segment_fixed_size: 0
    .sgpr_count:     30
    .sgpr_spill_count: 0
    .symbol:         _Z11vq_finalizePK15HIP_vector_typeIjLj4EEPKdPKiPf.kd
    .uniform_work_group_size: 1
    .uses_dynamic_stack: false
    .vgpr_count:     24
    .vgpr_spill_count: 0
    .wavefront_size: 64
